# attention: LDS fragment reads of the QK^T / PV MFMA chains issued 4 MFMAs ahead into spare quads with counted lgkmcnt (were ds_read -> lgkmcnt(0) -> mfma each)
# baseline (speedup 1.0000x reference)
.LBB0_404:
	v_add_u32_e32 v2, s7, v171
	ds_read_b128 v[216:219], v2
	ds_read_b128 v[232:235], v2 offset:512
	ds_read_b128 v[236:239], v2 offset:2048
	ds_read_b128 v[242:245], v2 offset:2560
	s_waitcnt lgkmcnt(3)
	v_mfma_f32_32x32x16_bf16 v[80:95], v[216:219], v[112:115], v[48:63]
	ds_read_b128 v[246:249], v2 offset:4096
	s_waitcnt lgkmcnt(3)
	v_mfma_f32_32x32x16_bf16 v[96:111], v[232:235], v[112:115], v[48:63]
	ds_read_b128 v[216:219], v2 offset:4608
	s_waitcnt lgkmcnt(3)
	v_mfma_f32_32x32x16_bf16 v[80:95], v[236:239], v[116:119], v[80:95]
	ds_read_b128 v[232:235], v2 offset:6656
	s_waitcnt lgkmcnt(3)
	v_mfma_f32_32x32x16_bf16 v[96:111], v[242:245], v[116:119], v[96:111]
	ds_read_b128 v[236:239], v2 offset:6144
	s_waitcnt lgkmcnt(3)
	v_mfma_f32_32x32x16_bf16 v[80:95], v[246:249], v[120:123], v[80:95]
	s_waitcnt lgkmcnt(2)
	v_mfma_f32_32x32x16_bf16 v[96:111], v[216:219], v[120:123], v[96:111]
	s_waitcnt lgkmcnt(1)
	v_mfma_f32_32x32x16_bf16 v[96:111], v[232:235], v[124:127], v[96:111]
	s_waitcnt lgkmcnt(0)
	v_mfma_f32_32x32x16_bf16 v[80:95], v[236:239], v[124:127], v[80:95]
	s_nop 8
	v_max_f32_e32 v0, v96, v96
	s_nop 1
	v_max_f32_e32 v3, v80, v80
	v_max_f32_e32 v0, v3, v0
	v_max3_f32 v0, v0, v81, v97
	v_max3_f32 v0, v0, v82, v98
	v_max3_f32 v0, v0, v83, v99
	v_max3_f32 v0, v0, v84, v100
	v_max3_f32 v0, v0, v85, v101
	v_max3_f32 v0, v0, v86, v102
	v_max3_f32 v0, v0, v87, v103
	v_max3_f32 v0, v0, v88, v104
	v_max3_f32 v0, v0, v89, v105
	v_max3_f32 v0, v0, v90, v106
	v_max3_f32 v0, v0, v91, v107
	v_max3_f32 v0, v0, v92, v108
	v_max3_f32 v0, v0, v93, v109
	v_max3_f32 v0, v0, v94, v110
	v_max3_f32 v0, v0, v95, v111
	v_mov_b32_e32 v3, v0
	s_nop 1
	v_permlane32_swap_b32_e32 v0, v3
	v_max_f32_e32 v3, v3, v3
	v_max_f32_e32 v0, v0, v0
	v_max_f32_e32 v0, v0, v3
	v_cmp_lt_f32_e32 vcc, s31, v0
	s_cbranch_vccnz .LBB0_409
	v_mov_b64_e32 v[78:79], v[62:63]
	v_mov_b32_e32 v3, 0
	v_mov_b64_e32 v[76:77], v[60:61]
	v_mov_b64_e32 v[74:75], v[58:59]
	v_mov_b64_e32 v[72:73], v[56:57]
	v_mov_b64_e32 v[70:71], v[54:55]
	v_mov_b64_e32 v[68:69], v[52:53]
	v_mov_b64_e32 v[66:67], v[50:51]
	v_mov_b64_e32 v[64:65], v[48:49]
.LBB0_406:
	v_exp_f32_e32 v15, v80
	v_exp_f32_e32 v141, v96
	v_exp_f32_e32 v0, v81
	v_exp_f32_e32 v12, v97
	v_exp_f32_e32 v142, v98
	v_add_f32_e32 v13, v141, v15
	v_exp_f32_e32 v96, v99
	v_pk_add_f32 v[4:5], v[12:13], v[0:1]
	v_exp_f32_e32 v13, v82
	v_pk_add_f32 v[6:7], v[4:5], v[4:5] op_sel_hi:[0,1]
	v_exp_f32_e32 v6, v83
	v_exp_f32_e32 v82, v101
	v_add_f32_e32 v97, v142, v13
	v_exp_f32_e32 v98, v107
	v_pk_add_f32 v[4:5], v[96:97], v[6:7]
	v_exp_f32_e32 v7, v84
	v_pk_add_f32 v[8:9], v[4:5], v[4:5] op_sel_hi:[0,1]
	v_exp_f32_e32 v97, v100
	v_exp_f32_e32 v8, v85
	v_exp_f32_e32 v84, v103
	v_exp_f32_e32 v100, v109
	v_add_f32_e32 v83, v97, v7
	v_pk_add_f32 v[4:5], v[82:83], v[8:9]
	v_exp_f32_e32 v9, v86
	v_pk_add_f32 v[10:11], v[4:5], v[4:5] op_sel_hi:[0,1]
	v_exp_f32_e32 v83, v102
	v_exp_f32_e32 v10, v87
	v_exp_f32_e32 v86, v105
	v_exp_f32_e32 v102, v111
	v_add_f32_e32 v85, v83, v9
	v_pk_add_f32 v[4:5], v[84:85], v[10:11]
	v_exp_f32_e32 v11, v88
	v_pk_add_f32 v[80:81], v[4:5], v[4:5] op_sel_hi:[0,1]
	v_exp_f32_e32 v85, v104
	v_exp_f32_e32 v80, v89
	v_cvt_pk_bf16_f32 v82, v97, v82
	v_cvt_pk_bf16_f32 v83, v83, v84
	v_add_f32_e32 v87, v85, v11
	v_pk_add_f32 v[4:5], v[86:87], v[80:81]
	v_exp_f32_e32 v81, v90
	v_pk_add_f32 v[88:89], v[4:5], v[4:5] op_sel_hi:[0,1]
	v_exp_f32_e32 v87, v106
	v_exp_f32_e32 v88, v91
	v_cvt_pk_bf16_f32 v84, v85, v86
	v_add_f32_e32 v99, v87, v81
	v_pk_add_f32 v[4:5], v[98:99], v[88:89]
	v_exp_f32_e32 v89, v92
	v_pk_add_f32 v[90:91], v[4:5], v[4:5] op_sel_hi:[0,1]
	v_exp_f32_e32 v99, v108
	v_exp_f32_e32 v90, v93
	v_cvt_pk_bf16_f32 v85, v87, v98
	v_add_f32_e32 v101, v99, v89
	v_pk_add_f32 v[4:5], v[100:101], v[90:91]
	v_exp_f32_e32 v91, v94
	v_pk_add_f32 v[92:93], v[4:5], v[4:5] op_sel_hi:[0,1]
	v_exp_f32_e32 v94, v110
	v_exp_f32_e32 v92, v95
	v_cvt_pk_bf16_f32 v86, v99, v100
	v_add_f32_e32 v103, v94, v91
	v_pk_add_f32 v[4:5], v[102:103], v[92:93]
	v_cvt_pk_bf16_f32 v87, v94, v102
	v_add_f32_e32 v4, v4, v5
	v_add_f32_e32 v14, v3, v4
	v_add_u32_e32 v3, s7, v170
	v_cvt_pk_bf16_f32 v4, v15, v0
	v_cvt_pk_bf16_f32 v5, v13, v6
	v_cvt_pk_bf16_f32 v6, v7, v8
	v_cvt_pk_bf16_f32 v7, v9, v10
	v_cvt_pk_bf16_f32 v8, v11, v80
	v_cvt_pk_bf16_f32 v9, v81, v88
	v_cvt_pk_bf16_f32 v10, v89, v90
	v_cvt_pk_bf16_f32 v11, v91, v92
	s_waitcnt vmcnt(0)
	ds_read_b64_tr_b16 v[216:217], v3 offset:32768
	ds_read_b64_tr_b16 v[218:219], v3 offset:33280
	ds_read_b64_tr_b16 v[232:233], v3 offset:33792
	ds_read_b64_tr_b16 v[234:235], v3 offset:34304
	ds_read_b64_tr_b16 v[236:237], v3 offset:34816
	ds_read_b64_tr_b16 v[238:239], v3 offset:35328
	ds_read_b64_tr_b16 v[242:243], v3 offset:35840
	ds_read_b64_tr_b16 v[244:245], v3 offset:36352
	s_waitcnt lgkmcnt(6)
	v_mfma_f32_32x32x16_bf16 v[32:47], v[4:7], v[216:219], v[32:47]
	ds_read_b64_tr_b16 v[246:247], v3 offset:36864
	ds_read_b64_tr_b16 v[248:249], v3 offset:37376
	v_cvt_pk_bf16_f32 v80, v141, v12
	v_cvt_pk_bf16_f32 v81, v142, v96
	s_waitcnt lgkmcnt(6)
	v_mfma_f32_32x32x16_bf16 v[32:47], v[8:11], v[232:235], v[32:47]
	ds_read_b64_tr_b16 v[216:217], v3 offset:37888
	ds_read_b64_tr_b16 v[218:219], v3 offset:38400
	s_waitcnt lgkmcnt(6)
	v_mfma_f32_32x32x16_bf16 v[32:47], v[80:83], v[236:239], v[32:47]
	ds_read_b64_tr_b16 v[232:233], v3 offset:38912
	ds_read_b64_tr_b16 v[234:235], v3 offset:39424
	s_waitcnt lgkmcnt(6)
	v_mfma_f32_32x32x16_bf16 v[32:47], v[84:87], v[242:245], v[32:47]
	ds_read_b64_tr_b16 v[236:237], v3 offset:39936
	ds_read_b64_tr_b16 v[238:239], v3 offset:40448
	s_waitcnt lgkmcnt(6)
	v_mfma_f32_32x32x16_bf16 v[16:31], v[4:7], v[246:249], v[16:31]
	ds_read_b128 v[242:245], v2 offset:8192
	s_waitcnt lgkmcnt(5)
	v_mfma_f32_32x32x16_bf16 v[16:31], v[8:11], v[216:219], v[16:31]
	ds_read_b128 v[246:249], v2 offset:8704
	s_waitcnt lgkmcnt(4)
	v_mfma_f32_32x32x16_bf16 v[16:31], v[80:83], v[232:235], v[16:31]
	ds_read_b128 v[216:219], v2 offset:10240
	s_waitcnt lgkmcnt(3)
	v_mfma_f32_32x32x16_bf16 v[16:31], v[84:87], v[236:239], v[16:31]
	ds_read_b128 v[232:235], v2 offset:10752
	s_waitcnt lgkmcnt(3)
	v_mfma_f32_32x32x16_bf16 v[80:95], v[242:245], v[112:115], v[64:79]
	ds_read_b128 v[236:239], v2 offset:12288
	s_waitcnt lgkmcnt(3)
	v_mfma_f32_32x32x16_bf16 v[64:79], v[246:249], v[112:115], v[64:79]
	ds_read_b128 v[242:245], v2 offset:12800
	s_waitcnt lgkmcnt(3)
	v_mfma_f32_32x32x16_bf16 v[80:95], v[216:219], v[116:119], v[80:95]
	ds_read_b128 v[246:249], v2 offset:14848
	s_waitcnt lgkmcnt(3)
	v_mfma_f32_32x32x16_bf16 v[64:79], v[232:235], v[116:119], v[64:79]
	ds_read_b128 v[216:219], v2 offset:14336
	s_waitcnt lgkmcnt(3)
	v_mfma_f32_32x32x16_bf16 v[80:95], v[236:239], v[120:123], v[80:95]
	s_waitcnt lgkmcnt(2)
	v_mfma_f32_32x32x16_bf16 v[64:79], v[242:245], v[120:123], v[64:79]
	s_waitcnt lgkmcnt(1)
	v_mfma_f32_32x32x16_bf16 v[64:79], v[246:249], v[124:127], v[64:79]
	s_waitcnt lgkmcnt(0)
	v_mfma_f32_32x32x16_bf16 v[80:95], v[216:219], v[124:127], v[80:95]
	s_nop 8
	v_max_f32_e32 v0, v64, v64
	s_nop 1
	v_max_f32_e32 v2, v80, v80
	v_max_f32_e32 v0, v2, v0
	v_max3_f32 v0, v0, v81, v65
	v_max3_f32 v0, v0, v82, v66
	v_max3_f32 v0, v0, v83, v67
	v_max3_f32 v0, v0, v84, v68
	v_max3_f32 v0, v0, v85, v69
	v_max3_f32 v0, v0, v86, v70
	v_max3_f32 v0, v0, v87, v71
	v_max3_f32 v0, v0, v88, v72
	v_max3_f32 v0, v0, v89, v73
	v_max3_f32 v0, v0, v90, v74
	v_max3_f32 v0, v0, v91, v75
	v_max3_f32 v0, v0, v92, v76
	v_max3_f32 v0, v0, v93, v77
	v_max3_f32 v0, v0, v94, v78
	v_max3_f32 v0, v0, v95, v79
	v_mov_b32_e32 v2, v0
	s_nop 1
	v_permlane32_swap_b32_e32 v0, v2
	v_max_f32_e32 v2, v2, v2
	v_max_f32_e32 v0, v0, v0
	v_max_f32_e32 v0, v0, v2
	v_cmp_lt_f32_e32 vcc, s31, v0
	s_cbranch_vccnz .LBB0_412
.LBB0_407:
	v_exp_f32_e32 v0, v80
	v_exp_f32_e32 v11, v81
	v_exp_f32_e32 v96, v82
	v_exp_f32_e32 v98, v83
	v_exp_f32_e32 v84, v84
	v_exp_f32_e32 v85, v85
	v_exp_f32_e32 v86, v86
	v_exp_f32_e32 v87, v87
	v_exp_f32_e32 v7, v64
	v_exp_f32_e32 v15, v65
	v_exp_f32_e32 v97, v66
	v_exp_f32_e32 v99, v67
	v_cvt_pk_bf16_f32 v64, v0, v11
	v_cvt_pk_bf16_f32 v65, v96, v98
	v_cvt_pk_bf16_f32 v66, v84, v85
	v_cvt_pk_bf16_f32 v67, v86, v87
	ds_read_b64_tr_b16 v[80:81], v3 offset:40960
	ds_read_b64_tr_b16 v[82:83], v3 offset:41472
	v_exp_f32_e32 v88, v88
	v_exp_f32_e32 v89, v89
	v_exp_f32_e32 v13, v90
	v_exp_f32_e32 v10, v91
	v_exp_f32_e32 v9, v92
	v_exp_f32_e32 v6, v93
	v_exp_f32_e32 v5, v94
	v_exp_f32_e32 v2, v95
	s_waitcnt lgkmcnt(0)
	v_mfma_f32_32x32x16_bf16 v[32:47], v[64:67], v[80:83], v[32:47]
	v_exp_f32_e32 v100, v68
	v_exp_f32_e32 v101, v69
	v_exp_f32_e32 v102, v70
	v_exp_f32_e32 v103, v71
	v_cvt_pk_bf16_f32 v68, v88, v89
	v_cvt_pk_bf16_f32 v69, v13, v10
	v_cvt_pk_bf16_f32 v70, v9, v6
	v_cvt_pk_bf16_f32 v71, v5, v2
	ds_read_b64_tr_b16 v[80:81], v3 offset:41984
	ds_read_b64_tr_b16 v[82:83], v3 offset:42496
	s_waitcnt lgkmcnt(0)
	v_mfma_f32_32x32x16_bf16 v[32:47], v[68:71], v[80:83], v[32:47]
	v_exp_f32_e32 v104, v72
	v_exp_f32_e32 v105, v73
	v_exp_f32_e32 v90, v74
	v_exp_f32_e32 v12, v75
	v_cvt_pk_bf16_f32 v72, v7, v15
	v_cvt_pk_bf16_f32 v73, v97, v99
	v_cvt_pk_bf16_f32 v74, v100, v101
	v_cvt_pk_bf16_f32 v75, v102, v103
	ds_read_b64_tr_b16 v[80:81], v3 offset:43008
	ds_read_b64_tr_b16 v[82:83], v3 offset:43520
	v_exp_f32_e32 v91, v76
	v_exp_f32_e32 v8, v77
	v_exp_f32_e32 v92, v78
	v_exp_f32_e32 v4, v79
	s_waitcnt lgkmcnt(0)
	v_mfma_f32_32x32x16_bf16 v[32:47], v[72:75], v[80:83], v[32:47]
	v_cvt_pk_bf16_f32 v76, v104, v105
	v_cvt_pk_bf16_f32 v77, v90, v12
	v_cvt_pk_bf16_f32 v78, v91, v8
	v_cvt_pk_bf16_f32 v79, v92, v4
	ds_read_b64_tr_b16 v[216:217], v3 offset:44032
	ds_read_b64_tr_b16 v[218:219], v3 offset:44544
	ds_read_b64_tr_b16 v[232:233], v3 offset:45056
	ds_read_b64_tr_b16 v[234:235], v3 offset:45568
	ds_read_b64_tr_b16 v[236:237], v3 offset:46080
	ds_read_b64_tr_b16 v[238:239], v3 offset:46592
	ds_read_b64_tr_b16 v[242:243], v3 offset:47104
	ds_read_b64_tr_b16 v[244:245], v3 offset:47616
	s_waitcnt lgkmcnt(6)
	v_mfma_f32_32x32x16_bf16 v[32:47], v[76:79], v[216:219], v[32:47]
	ds_read_b64_tr_b16 v[246:247], v3 offset:48128
	ds_read_b64_tr_b16 v[248:249], v3 offset:48640
	s_waitcnt lgkmcnt(6)
	v_mfma_f32_32x32x16_bf16 v[16:31], v[64:67], v[232:235], v[16:31]
	s_waitcnt lgkmcnt(4)
	v_mfma_f32_32x32x16_bf16 v[16:31], v[68:71], v[236:239], v[16:31]
	s_waitcnt lgkmcnt(2)
	v_mfma_f32_32x32x16_bf16 v[16:31], v[72:75], v[242:245], v[16:31]
	s_waitcnt lgkmcnt(0)
	v_mfma_f32_32x32x16_bf16 v[16:31], v[76:79], v[246:249], v[16:31]
	v_add_f32_e32 v0, v7, v0
	v_add_f32_e32 v11, v15, v11
	v_add_f32_e32 v0, 0, v0
	v_add_f32_e32 v70, v97, v96
	v_add_f32_e32 v0, v11, v0
	v_add_f32_e32 v69, v99, v98
	v_add_f32_e32 v0, v70, v0
	v_add_f32_e32 v68, v100, v84
	v_add_f32_e32 v0, v69, v0
	v_add_f32_e32 v67, v101, v85
	v_add_f32_e32 v0, v68, v0
	v_add_f32_e32 v66, v102, v86
	v_add_f32_e32 v0, v67, v0
	v_add_f32_e32 v65, v103, v87
	v_add_f32_e32 v0, v66, v0
	v_add_f32_e32 v64, v104, v88
	v_add_f32_e32 v0, v65, v0
	v_add_f32_e32 v3, v105, v89
	v_add_f32_e32 v0, v64, v0
	v_add_f32_e32 v13, v90, v13
	v_add_f32_e32 v11, v3, v0
	v_pk_add_f32 v[10:11], v[12:13], v[10:11]
	v_add_f32_e32 v9, v91, v9
	v_pk_add_f32 v[10:11], v[10:11], v[10:11] op_sel_hi:[0,1]
	v_mov_b32_e32 v7, v11
	v_pk_add_f32 v[6:7], v[8:9], v[6:7]
	v_add_f32_e32 v5, v92, v5
	v_pk_add_f32 v[6:7], v[6:7], v[6:7] op_sel_hi:[0,1]
	v_mov_b32_e32 v3, v7
	v_pk_add_f32 v[2:3], v[4:5], v[2:3]
	s_movk_i32 s7, 0x4000
	v_add_f32_e32 v0, v2, v3
	v_add_f32_e32 v0, v14, v0
	v_mov_b32_e32 v2, v0
	s_nop 1
	v_permlane32_swap_b32_e32 v0, v2
	v_add_f32_e32 v0, v0, v2
	v_add_f32_e32 v129, v129, v0
	s_mov_b64 s[4:5], 0
	s_and_b64 vcc, exec, s[2:3]
	s_barrier
	s_cbranch_vccnz .LBB0_416
	s_mov_b64 s[2:3], -1
	s_andn2_b64 vcc, exec, s[4:5]
	s_cbranch_vccz .LBB0_403
	s_branch .LBB0_404

.LBB0_428:
	v_add_u32_e32 v2, s29, v171
	ds_read_b128 v[4:7], v2
	s_add_i32 s9, s28, s27
	s_cmp_gt_u32 s27, s16
	s_waitcnt lgkmcnt(0)
	v_mfma_f32_32x32x16_bf16 v[80:95], v[4:7], v[144:147], v[48:63]
	ds_read_b128 v[216:219], v2 offset:512
	ds_read_b128 v[232:235], v2 offset:2048
	ds_read_b128 v[236:239], v2 offset:2560
	ds_read_b128 v[242:245], v2 offset:4096
	s_waitcnt lgkmcnt(3)
	v_mfma_f32_32x32x16_bf16 v[96:111], v[216:219], v[144:147], v[48:63]
	ds_read_b128 v[246:249], v2 offset:4608
	s_waitcnt lgkmcnt(3)
	v_mfma_f32_32x32x16_bf16 v[80:95], v[232:235], v[148:151], v[80:95]
	ds_read_b128 v[216:219], v2 offset:6144
	s_waitcnt lgkmcnt(3)
	v_mfma_f32_32x32x16_bf16 v[96:111], v[236:239], v[148:151], v[96:111]
	ds_read_b128 v[232:235], v2 offset:6656
	s_waitcnt lgkmcnt(3)
	v_mfma_f32_32x32x16_bf16 v[80:95], v[242:245], v[152:155], v[80:95]
	s_waitcnt lgkmcnt(2)
	v_mfma_f32_32x32x16_bf16 v[96:111], v[246:249], v[152:155], v[96:111]
	s_waitcnt lgkmcnt(1)
	v_mfma_f32_32x32x16_bf16 v[80:95], v[216:219], v[156:159], v[80:95]
	s_waitcnt lgkmcnt(0)
	v_mfma_f32_32x32x16_bf16 v[96:111], v[232:235], v[156:159], v[96:111]
	s_cbranch_scc1 .LBB0_441
	s_cmp_lt_i32 s9, 4
	s_cbranch_scc1 .LBB0_435
	s_nop 8
	v_mov_b64_e32 v[64:65], v[96:97]
	v_mov_b64_e32 v[126:127], v[94:95]
	s_mov_b64 vcc, 0
	s_cmp_eq_u32 s9, 4
	s_mov_b64 s[12:13], 0
	v_mov_b64_e32 v[66:67], v[98:99]
	v_mov_b64_e32 v[68:69], v[100:101]
	v_mov_b64_e32 v[70:71], v[102:103]
	v_mov_b64_e32 v[72:73], v[104:105]
	v_mov_b64_e32 v[74:75], v[106:107]
	v_mov_b64_e32 v[76:77], v[108:109]
	v_mov_b64_e32 v[78:79], v[110:111]
	v_mov_b64_e32 v[124:125], v[92:93]
	v_mov_b64_e32 v[122:123], v[90:91]
	v_mov_b64_e32 v[120:121], v[88:89]
	v_mov_b64_e32 v[118:119], v[86:87]
	v_mov_b64_e32 v[116:117], v[84:85]
	v_mov_b64_e32 v[114:115], v[82:83]
	v_mov_b64_e32 v[112:113], v[80:81]
	s_cbranch_scc0 .LBB0_432
	v_cndmask_b32_e64 v78, v110, v215, s[0:1]
	v_mov_b32_e32 v79, v111
	v_cndmask_b32_e64 v0, v80, v215, s[40:41]
	v_cndmask_b32_e64 v64, v96, v215, s[42:43]
	v_cndmask_b32_e64 v65, v97, v215, s[46:47]
	v_cndmask_b32_e64 v66, v98, v215, s[50:51]
	v_cndmask_b32_e64 v67, v99, v215, s[54:55]
	v_cndmask_b32_e64 v68, v100, v215, s[58:59]
	v_cndmask_b32_e64 v69, v101, v215, s[62:63]
	v_cndmask_b32_e64 v70, v102, v215, s[66:67]
	v_cndmask_b32_e64 v71, v103, v215, s[70:71]
	v_cndmask_b32_e64 v72, v104, v215, s[74:75]
	v_cndmask_b32_e64 v73, v105, v215, s[78:79]
	v_cndmask_b32_e64 v74, v106, v215, s[82:83]
	v_cndmask_b32_e64 v75, v107, v215, s[86:87]
	v_cndmask_b32_e64 v76, v108, v215, s[90:91]
	v_cndmask_b32_e64 v77, v109, v215, s[94:95]
	v_mov_b64_e32 v[142:143], v[78:79]
	v_cndmask_b32_e64 v113, v215, v81, s[44:45]
	v_cndmask_b32_e64 v112, v0, v80, s[44:45]
	v_cndmask_b32_e64 v114, v82, v215, s[48:49]
	v_cndmask_b32_e64 v115, v83, v215, s[52:53]
	v_cndmask_b32_e64 v116, v84, v215, s[56:57]
	v_cndmask_b32_e64 v117, v85, v215, s[60:61]
	v_cndmask_b32_e64 v118, v86, v215, s[64:65]
	v_cndmask_b32_e64 v119, v87, v215, s[68:69]
	v_cndmask_b32_e64 v120, v88, v215, s[72:73]
	v_cndmask_b32_e64 v121, v89, v215, s[76:77]
	v_cndmask_b32_e64 v122, v90, v215, s[80:81]
	v_cndmask_b32_e64 v123, v91, v215, s[84:85]
	v_cndmask_b32_e64 v124, v92, v215, s[88:89]
	v_cndmask_b32_e64 v125, v93, v215, s[92:93]
	v_cndmask_b32_e64 v126, v94, v215, s[96:97]
	v_cndmask_b32_e64 v127, v95, v215, s[4:5]
	s_and_b64 s[12:13], s[6:7], exec
	v_mov_b64_e32 v[140:141], v[76:77]
	v_mov_b64_e32 v[138:139], v[74:75]
	v_mov_b64_e32 v[136:137], v[72:73]
	v_mov_b64_e32 v[134:135], v[70:71]
	v_mov_b64_e32 v[132:133], v[68:69]
	v_mov_b64_e32 v[130:131], v[66:67]
	v_mov_b64_e32 v[128:129], v[64:65]
